# P5 phase interleave: half the workgroups run the HBM-bound hy_finish tiles before the latency-bound ml_out items
# speedup vs baseline: 1.0065x; 1.0065x over previous
.Lp5_pre:
	s_cmp_eq_u32 s32, 3
	s_cbranch_scc1 .Lp5_a
	s_bfe_u32 s32, s92, 0x10003
.Lp5_a:
	s_cmpk_lt_i32 s92, 0x400
	v_readlane_b32 s4, v252, 2
	s_cselect_b64 s[0:1], -1, 0
	s_lshl_b32 s2, s97, 4
	v_readlane_b32 s6, v252, 4
	v_writelane_b32 v253, s2, 33
	v_readlane_b32 s7, v252, 5
	s_add_u32 s2, s6, 0x3d700000
	v_lshlrev_b32_e32 v2, 5, v0
	v_writelane_b32 v253, s2, 34
	s_addc_u32 s2, s7, 0
	v_and_b32_e32 v27, 0x60, v2
	s_waitcnt vmcnt(0)
	v_mov_b32_e32 v10, 0
	v_writelane_b32 v253, s2, 35
	s_cmpk_gt_i32 s92, 0x3ff
	s_mov_b32 s3, 0
	v_mov_b32_e32 v2, 0
	v_lshlrev_b32_e32 v150, 1, v27
	v_mov_b32_e32 v11, v10
	v_mov_b32_e32 v12, v10
	v_mov_b32_e32 v13, v10
	v_mov_b32_e32 v14, v10
	v_mov_b32_e32 v15, v10
	v_mov_b32_e32 v16, v10
	v_mov_b32_e32 v17, v10
	v_mov_b32_e32 v18, v10
	v_mov_b32_e32 v19, v10
	v_mov_b32_e32 v20, v10
	v_mov_b32_e32 v21, v10
	v_mov_b32_e32 v22, v10
	v_mov_b32_e32 v23, v10
	v_mov_b32_e32 v24, v10
	v_mov_b32_e32 v25, v10
	v_mov_b32_e32 v3, 0
	v_mov_b32_e32 v4, 0
	v_mov_b32_e32 v5, 0
	v_mov_b32_e32 v6, 0
	v_mov_b32_e32 v7, 0
	v_mov_b32_e32 v8, 0
	v_mov_b32_e32 v9, 0
	v_readlane_b32 s5, v252, 3
	s_cbranch_scc1 .LBB0_835
	s_lshl_b32 s2, s92, 4
	v_readlane_b32 s8, v252, 2
	s_and_b32 s6, s2, 0xffffff80
	v_lshrrev_b32_e32 v1, 2, v0
	v_readlane_b32 s10, v252, 4
	v_readlane_b32 s11, v252, 5
	v_or_b32_e32 v4, s6, v1
	s_movk_i32 s2, 0x3200
	v_mov_b64_e32 v[2:3], s[10:11]
	v_mad_i64_i32 v[2:3], s[4:5], v4, s2, v[2:3]
	s_and_b32 s4, s92, 7
	s_lshl_b32 s2, s4, 8
	v_lshl_add_u64 v[2:3], v[2:3], 0, s[2:3]
	v_mov_b32_e32 v151, 0
	v_lshl_add_u64 v[2:3], v[2:3], 0, v[150:151]
	s_mov_b64 s[2:3], 0x1eb00400
	v_lshl_add_u64 v[28:29], v[2:3], 0, s[2:3]
	s_lshl_b32 s2, s4, 14
	s_ashr_i32 s3, s6, 31
	s_add_u32 s2, s2, s6
	s_addc_u32 s3, 0, s3
	s_lshl_b64 s[2:3], s[2:3], 7
	v_readlane_b32 s4, v253, 34
	s_add_u32 s2, s4, s2
	v_readlane_b32 s4, v253, 35
	v_mov_b32_e32 v6, v206
	s_addc_u32 s3, s4, s3
	v_readlane_b32 s4, v253, 33
	v_mov_b32_e32 v5, v151
	v_readlane_b32 s9, v252, 3
	v_and_or_b32 v4, v6, 15, s4
	v_ashrrev_i32_e32 v6, 1, v6
	v_lshlrev_b64 v[4:5], 7, v[4:5]
	v_and_b32_e32 v6, -8, v6
	v_lshl_add_u64 v[4:5], s[2:3], 0, v[4:5]
	v_ashrrev_i32_e32 v7, 31, v6
	s_mov_b32 s2, 0x1eb00000
	v_lshl_add_u64 v[30:31], v[6:7], 1, v[4:5]
	v_add_co_u32_e32 v32, vcc, s2, v2
	s_nop 1
	v_addc_co_u32_e32 v33, vcc, 0, v3, vcc
	global_load_dwordx4 v[6:9], v[30:31], off offset:64
	global_load_dwordx4 v[10:13], v[32:33], off offset:1024
	global_load_dwordx4 v[14:17], v[28:29], off offset:16
	global_load_dwordx4 v[18:21], v[28:29], off offset:32
	global_load_dwordx4 v[2:5], v[30:31], off
	global_load_dwordx4 v[22:25], v[28:29], off offset:48
.LBB0_835:
	s_andn2_b64 vcc, exec, s[0:1]
	s_cbranch_vccnz .LBB0_1002
	v_writelane_b32 v253, s64, 36
	v_readlane_b32 s76, v252, 2
	v_and_b32_e32 v154, 48, v206
	v_writelane_b32 v253, s65, 37
	v_writelane_b32 v253, s88, 16
	v_mov_b32_e32 v155, 0
	v_readlane_b32 s78, v252, 4
	v_writelane_b32 v253, s89, 17
	v_writelane_b32 v253, s90, 18
	v_writelane_b32 v253, s91, 19
	v_writelane_b32 v253, s92, 20
	v_writelane_b32 v253, s93, 21
	v_writelane_b32 v253, s94, 22
	v_writelane_b32 v253, s95, 23
	v_readlane_b32 s79, v252, 5
	v_cmp_eq_u32_e64 s[2:3], 0, v206
	s_mov_b64 s[0:1], 0x3e700000
	v_lshl_add_u64 v[38:39], s[78:79], 0, v[154:155]
	v_readlane_b32 s55, v253, 33
	v_writelane_b32 v253, s2, 38
	v_lshl_add_u64 v[156:157], v[38:39], 0, s[0:1]
	s_cmpk_lt_u32 s63, 0x80
	s_mul_i32 s0, s97, 0x600
	v_writelane_b32 v253, s3, 39
	v_cmp_gt_u32_e64 s[2:3], 2, v206
	s_cselect_b64 s[58:59], -1, 0
	s_add_i32 s33, s0, 0
	v_writelane_b32 v253, s2, 40
	s_add_u32 s56, s78, 0x1eb00000
	s_addc_u32 s57, s79, 0
	v_writelane_b32 v253, s3, 41
	v_cmp_gt_u32_e64 s[2:3], 4, v206
	v_lshlrev_b32_e32 v33, 1, v206
	s_cmp_lt_u32 s63, 64
	v_writelane_b32 v253, s2, 42
	s_cselect_b64 vcc, -1, 0
	v_xor_b32_e32 v35, 0x7f, v33
	v_writelane_b32 v253, s3, 43
	v_cmp_gt_u32_e64 s[2:3], 8, v206
	v_cndmask_b32_e32 v209, v35, v33, vcc
	s_and_b64 s[0:1], vcc, exec
	v_writelane_b32 v253, s2, 44
	s_cselect_b32 s0, 1, -1
	v_lshl_add_u32 v211, v209, 2, s33
	v_writelane_b32 v253, s3, 45
	v_cmp_gt_u32_e64 s[2:3], 32, v206
	v_add_u32_e32 v210, s0, v209
	v_lshl_add_u32 v212, s0, 2, v211
	v_writelane_b32 v253, s2, 46
	s_add_u32 s0, s78, 0x3fe48000
	v_and_b32_e32 v153, 15, v0
	v_writelane_b32 v253, s3, 47
	v_writelane_b32 v253, s0, 48
	s_addc_u32 s0, s79, 0
	v_writelane_b32 v253, s0, 49
	s_lshl_b32 s0, s97, 10
	v_lshrrev_b32_e32 v29, 4, v206
	v_writelane_b32 v253, s0, 50
	s_lshl_b32 s0, s97, 8
	v_or_b32_e32 v208, s55, v153
	v_lshlrev_b32_e32 v214, 2, v29
	v_writelane_b32 v253, s97, 28
	s_add_i32 s0, s0, 0
	v_writelane_b32 v253, s0, 24
	v_cmp_ge_u32_e64 s[0:1], v214, v208
	v_lshrrev_b32_e32 v1, 2, v0
	v_mul_u32_u24_e32 v27, 0x110, v27
	v_writelane_b32 v253, s0, 25
	v_lshlrev_b32_e32 v33, 1, v1
	v_add3_u32 v213, 0, v27, v33
	v_writelane_b32 v253, s1, 26
	v_cmp_le_u32_e64 s[0:1], v214, v208
	v_or_b32_e32 v27, 1, v214
	s_cmpk_lt_u32 s63, 0x100
	v_writelane_b32 v253, s0, 29
	s_cselect_b64 s[64:65], -1, 0
	s_cmpk_gt_u32 s63, 0x7f
	v_writelane_b32 v253, s1, 30
	v_cmp_ge_u32_e64 s[0:1], v27, v208
	v_or_b32_e32 v27, 2, v214
	s_cselect_b64 s[66:67], -1, 0
	v_writelane_b32 v253, s0, 14
	s_cmpk_lt_u32 s63, 0x180
	s_cselect_b64 s[68:69], -1, 0
	v_writelane_b32 v253, s1, 15
	v_cmp_lt_u32_e64 s[0:1], v214, v208
	s_cmpk_gt_u32 s63, 0xff
	s_mov_b32 s54, s92
	v_writelane_b32 v253, s0, 51
	s_cselect_b64 s[70:71], -1, 0
	s_cmpk_lt_u32 s63, 0x200
	v_writelane_b32 v253, s1, 52
	v_cmp_ge_u32_e64 s[0:1], v27, v208
	s_mov_b64 s[52:53], 0x3b700000
	v_lshlrev_b32_e32 v154, 5, v29
	v_writelane_b32 v253, s0, 53
	s_mul_i32 s50, s97, 0xfffffa04
	s_cselect_b64 s[72:73], -1, 0
	v_writelane_b32 v253, s1, 54
	v_cmp_le_u32_e64 s[0:1], v27, v208
	v_or_b32_e32 v27, 3, v214
	s_cmpk_gt_u32 s63, 0x17f
	v_writelane_b32 v253, s0, 55
	v_lshl_add_u64 v[158:159], v[38:39], 0, s[52:53]
	v_lshl_add_u64 v[38:39], s[78:79], 0, v[154:155]
	v_writelane_b32 v253, s1, 56
	v_cmp_ge_u32_e64 s[0:1], v27, v208
	s_mov_b64 s[52:53], 0x3fda8000
	s_cselect_b64 s[74:75], -1, 0
	v_writelane_b32 v253, s0, 57
	v_lshl_add_u64 v[160:161], v[38:39], 0, s[52:53]
	s_add_u32 s52, s78, 0x1eb01040
	v_writelane_b32 v253, s1, 58
	v_cmp_le_u32_e64 s[0:1], v27, v208
	v_or_b32_e32 v27, 16, v214
	s_addc_u32 s53, s79, 0
	v_writelane_b32 v253, s0, 59
	s_mov_b32 s51, s63
	v_lshlrev_b32_e32 v152, 6, v153
	v_writelane_b32 v253, s1, 60
	v_cmp_ge_u32_e64 s[0:1], v27, v208
	v_or_b32_e32 v26, 0x800, v152
	v_lshlrev_b32_e32 v162, 1, v26
	v_writelane_b32 v253, s0, 61
	v_lshlrev_b32_e32 v31, 3, v29
	v_or_b32_e32 v28, 0xc00, v152
	v_writelane_b32 v253, s1, 62
	v_cmp_le_u32_e64 s[0:1], v27, v208
	v_or_b32_e32 v27, 17, v214
	v_or_b32_e32 v30, 0x1000, v152
	v_writelane_b32 v253, s0, 63
	v_writelane_b32 v253, s51, 27
	v_or_b32_e32 v32, 0x1400, v152
	v_writelane_b32 v254, s1, 0
	v_cmp_ge_u32_e64 s[0:1], v27, v208
	v_or_b32_e32 v34, 0x1800, v152
	v_or_b32_e32 v36, 0x1c00, v152
	v_writelane_b32 v254, s0, 1
	v_mbcnt_lo_u32_b32 v26, -1, 0
	s_mov_b32 s60, 0
	v_writelane_b32 v254, s1, 2
	v_cmp_le_u32_e64 s[0:1], v27, v208
	v_or_b32_e32 v27, 18, v214
	v_cmp_gt_u32_e64 s[10:11], 16, v206
	v_writelane_b32 v254, s0, 3
	v_and_b32_e32 v215, 48, v0
	v_or_b32_e32 v217, s55, v214
	v_writelane_b32 v254, s1, 4
	v_cmp_ge_u32_e64 s[0:1], v27, v208
	v_lshlrev_b32_e32 v164, 1, v28
	v_lshlrev_b32_e32 v166, 1, v30
	v_writelane_b32 v254, s0, 5
	v_lshlrev_b32_e32 v168, 1, v32
	v_lshlrev_b32_e32 v170, 1, v34
	v_writelane_b32 v254, s1, 6
	v_cmp_le_u32_e64 s[0:1], v27, v208
	v_or_b32_e32 v27, 19, v214
	v_lshlrev_b32_e32 v172, 1, v36
	v_writelane_b32 v254, s0, 7
	s_movk_i32 s80, 0x3200
	v_mov_b32_e32 v218, 0x3ecc95a3
	v_writelane_b32 v254, s1, 8
	v_cmp_ge_u32_e64 s[0:1], v27, v208
	v_mbcnt_hi_u32_b32 v219, -1, v26
	v_mov_b32_e32 v220, 0x7f800000
	v_writelane_b32 v254, s0, 9
	v_mov_b32_e32 v221, 0x7fc00000
	v_mov_b32_e32 v222, 0xff800000
	v_writelane_b32 v254, s1, 10
	v_cmp_le_u32_e64 s[0:1], v27, v208
	v_or_b32_e32 v27, 32, v214
	v_readlane_b32 s77, v252, 3
	v_writelane_b32 v254, s0, 11
	s_nop 1
	v_writelane_b32 v254, s1, 12
	v_cmp_ge_u32_e64 s[0:1], v27, v208
	s_nop 1
	v_writelane_b32 v254, s0, 13
	s_nop 1
	v_writelane_b32 v254, s1, 14
	v_cmp_le_u32_e64 s[0:1], v27, v208
	v_or_b32_e32 v27, 33, v214
	s_nop 0
	v_writelane_b32 v254, s0, 15
	s_nop 1
	v_writelane_b32 v254, s1, 16
	v_cmp_ge_u32_e64 s[0:1], v27, v208
	s_nop 1
	v_writelane_b32 v254, s0, 17
	s_nop 1
	v_writelane_b32 v254, s1, 18
	v_cmp_le_u32_e64 s[0:1], v27, v208
	v_or_b32_e32 v27, 34, v214
	s_nop 0
	v_writelane_b32 v254, s0, 19
	s_nop 1
	v_writelane_b32 v254, s1, 20
	v_cmp_ge_u32_e64 s[0:1], v27, v208
	s_nop 1
	v_writelane_b32 v254, s0, 21
	s_nop 1
	v_writelane_b32 v254, s1, 22
	v_cmp_le_u32_e64 s[0:1], v27, v208
	v_or_b32_e32 v27, 35, v214
	s_nop 0
	v_writelane_b32 v254, s0, 23
	s_nop 1
	v_writelane_b32 v254, s1, 24
	v_cmp_ge_u32_e64 s[0:1], v27, v208
	s_nop 1
	v_writelane_b32 v254, s0, 25
	s_nop 1
	v_writelane_b32 v254, s1, 26
	v_cmp_le_u32_e64 s[0:1], v27, v208
	v_or_b32_e32 v27, 48, v214
	s_nop 0
	v_writelane_b32 v254, s0, 27
	s_nop 1
	v_writelane_b32 v254, s1, 28
	v_cmp_ge_u32_e64 s[0:1], v27, v208
	s_nop 1
	v_writelane_b32 v254, s0, 29
	s_nop 1
	v_writelane_b32 v254, s1, 30
	v_cmp_le_u32_e64 s[0:1], v27, v208
	v_or_b32_e32 v27, 49, v214
	s_nop 0
	v_writelane_b32 v254, s0, 31
	s_nop 1
	v_writelane_b32 v254, s1, 32
	v_cmp_ge_u32_e64 s[0:1], v27, v208
	s_nop 1
	v_writelane_b32 v254, s0, 33
	s_nop 1
	v_writelane_b32 v254, s1, 34
	v_cmp_le_u32_e64 s[0:1], v27, v208
	v_or_b32_e32 v27, 50, v214
	s_nop 0
	v_writelane_b32 v254, s0, 35
	s_nop 1
	v_writelane_b32 v254, s1, 36
	v_cmp_ge_u32_e64 s[0:1], v27, v208
	s_nop 1
	v_writelane_b32 v254, s0, 37
	s_nop 1
	v_writelane_b32 v254, s1, 38
	v_cmp_le_u32_e64 s[0:1], v27, v208
	v_or_b32_e32 v27, 51, v214
	s_nop 0
	v_writelane_b32 v254, s0, 39
	s_nop 1
	v_writelane_b32 v254, s1, 40
	v_cmp_ge_u32_e64 s[0:1], v27, v208
	s_nop 1
	v_writelane_b32 v254, s0, 41
	s_nop 1
	v_writelane_b32 v254, s1, 42
	v_cmp_le_u32_e64 s[0:1], v27, v208
	v_or_b32_e32 v27, 64, v214
	s_nop 0
	v_writelane_b32 v254, s0, 43
	s_nop 1
	v_writelane_b32 v254, s1, 44
	v_cmp_ge_u32_e64 s[0:1], v27, v208
	s_nop 1
	v_writelane_b32 v254, s0, 45
	s_nop 1
	v_writelane_b32 v254, s1, 46
	v_cmp_le_u32_e64 s[0:1], v27, v208
	v_or_b32_e32 v27, 0x41, v214
	s_nop 0
	v_writelane_b32 v254, s0, 47
	s_nop 1
	v_writelane_b32 v254, s1, 48
	v_cmp_ge_u32_e64 s[0:1], v27, v208
	s_nop 1
	v_writelane_b32 v254, s0, 49
	s_nop 1
	v_writelane_b32 v254, s1, 50
	v_cmp_le_u32_e64 s[0:1], v27, v208
	v_or_b32_e32 v27, 0x42, v214
	s_nop 0
	v_writelane_b32 v254, s0, 51
	s_nop 1
	v_writelane_b32 v254, s1, 52
	v_cmp_ge_u32_e64 s[0:1], v27, v208
	s_nop 1
	v_writelane_b32 v254, s0, 53
	s_nop 1
	v_writelane_b32 v254, s1, 54
	v_cmp_le_u32_e64 s[0:1], v27, v208
	v_or_b32_e32 v27, 0x43, v214
	v_cmp_ge_u32_e64 s[92:93], v27, v208
	v_cmp_le_u32_e64 s[94:95], v27, v208
	v_or_b32_e32 v27, 0x50, v214
	v_cmp_ge_u32_e64 s[96:97], v27, v208
	v_cmp_le_u32_e64 s[4:5], v27, v208
	v_or_b32_e32 v27, 0x51, v214
	v_writelane_b32 v254, s0, 55
	v_cmp_ge_u32_e64 s[6:7], v27, v208
	v_cmp_le_u32_e64 s[8:9], v27, v208
	v_or_b32_e32 v27, 0x52, v214
	v_writelane_b32 v254, s1, 56
	v_cmp_ge_u32_e64 s[12:13], v27, v208
	v_cmp_le_u32_e64 s[0:1], v27, v208
	v_or_b32_e32 v27, 0x53, v214
	v_cmp_ge_u32_e64 s[2:3], v27, v208
	v_cmp_le_u32_e64 s[14:15], v27, v208
	v_or_b32_e32 v27, 0x60, v214
	v_writelane_b32 v254, s52, 57
	v_cmp_ge_u32_e64 s[16:17], v27, v208
	v_cmp_le_u32_e64 s[18:19], v27, v208
	v_or_b32_e32 v27, 0x61, v214
	v_writelane_b32 v254, s53, 58
	s_add_u32 s52, s78, 0x2b700000
	v_cmp_ge_u32_e64 s[20:21], v27, v208
	v_cmp_le_u32_e64 s[22:23], v27, v208
	v_or_b32_e32 v27, 0x62, v214
	s_addc_u32 s53, s79, 0
	v_cmp_ge_u32_e64 s[24:25], v27, v208
	v_cmp_le_u32_e64 s[26:27], v27, v208
	v_or_b32_e32 v27, 0x63, v214
	v_writelane_b32 v254, s52, 59
	v_cmp_ge_u32_e64 s[28:29], v27, v208
	v_cmp_le_u32_e64 s[30:31], v27, v208
	v_or_b32_e32 v27, 0x70, v214
	v_writelane_b32 v254, s53, 60
	s_lshl_b32 s51, s55, 1
	v_cmp_ge_u32_e64 s[34:35], v27, v208
	v_cmp_le_u32_e64 s[36:37], v27, v208
	v_or_b32_e32 v27, 0x71, v214
	s_add_u32 s52, s56, s51
	v_writelane_b32 v254, s56, 61
	v_cmp_ge_u32_e64 s[38:39], v27, v208
	v_cmp_le_u32_e64 s[40:41], v27, v208
	v_or_b32_e32 v27, 0x72, v214
	v_writelane_b32 v254, s57, 62
	s_addc_u32 s53, s57, 0
	v_cmp_ge_u32_e64 s[42:43], v27, v208
	v_cmp_le_u32_e64 s[44:45], v27, v208
	v_or_b32_e32 v27, 0x73, v214
	v_writelane_b32 v254, s52, 63
	s_add_i32 s33, s33, s50
	s_mov_b32 s50, s54
	v_writelane_b32 v255, s53, 0
	v_cmp_ge_u32_e64 s[46:47], v27, v208
	v_cmp_le_u32_e64 s[48:49], v27, v208
	v_mul_u32_u24_e32 v27, 0x110, v153
	v_writelane_b32 v255, s33, 1
	v_writelane_b32 v253, s50, 31
	s_mov_b32 s33, s54
	v_add3_u32 v216, 0, v31, v27
	v_writelane_b32 v253, s51, 32
	v_writelane_b32 v255, s33, 2
	s_cmp_eq_u32 s32, 1
	s_cbranch_scc0 .Lp5_b
	s_mov_b32 s32, 2
	s_waitcnt vmcnt(0) lgkmcnt(0)
	s_branch .LBB0_977
.Lp5_b:
	s_branch .LBB0_838

.LBB0_979:
	s_cmp_eq_u32 s32, 3
	s_cbranch_scc0 .Lp5_d
	s_mov_b32 s32, 0
	s_branch .LBB0_1001

.LBB0_1001:
	v_readlane_b32 s56, v252, 59
	s_mov_b32 s92, s58
	s_cmp_eq_u32 s32, 2
	s_cbranch_scc0 .Lp5_c
	s_mov_b32 s32, 3
	s_branch .Lp5_pre
.Lp5_c:
.LBB0_1002:
	s_cmp_gt_i32 s61, 6
	s_cselect_b64 s[0:1], -1, 0
	s_and_b64 s[2:3], s[64:65], s[0:1]
	s_andn2_b64 vcc, exec, s[2:3]
	s_cbranch_vccnz .LBB0_1052
	s_waitcnt vmcnt(0)
	v_cmp_eq_u32_e32 vcc, 0, v0
	s_waitcnt vmcnt(0)
	s_barrier
	s_and_saveexec_b64 s[2:3], vcc
	s_cbranch_execz .LBB0_1051
	v_readlane_b32 s4, v252, 8
	s_waitcnt vmcnt(0) expcnt(0) lgkmcnt(0)
	s_nop 0
	v_mov_b32_e32 v1, s4
	ds_read_b32 v3, v1
	ds_read_b32 v1, v1 offset:4
	s_waitcnt lgkmcnt(1)
	v_cmp_ne_u32_e32 vcc, 0, v3
	s_cbranch_vccnz .LBB0_1019
	v_readlane_b32 s4, v252, 0
	v_readlane_b32 s5, v252, 1
	v_readlane_b32 s36, v252, 2
	s_load_dwordx2 s[8:9], s[4:5], 0x4
	v_readlane_b32 s38, v252, 4
	v_readlane_b32 s39, v252, 5
	s_add_u32 s4, s38, 0x4200
	s_addc_u32 s5, s39, 0
	s_add_u32 s6, s38, 0x4400
	s_addc_u32 s7, s39, 0
	s_waitcnt lgkmcnt(0)
	s_mul_i32 s33, s8, s62
	s_add_u32 s8, s38, 0x4500
	s_mul_i32 s33, s33, s9
	s_addc_u32 s9, s39, 0
	s_add_u32 s10, s38, 0x4600
	s_addc_u32 s11, s39, 0
	s_add_u32 s12, s38, 0x4700
	s_addc_u32 s13, s39, 0
	s_add_u32 s14, s38, 0x4800
	s_addc_u32 s15, s39, 0
	s_add_u32 s16, s38, 0x4900
	s_addc_u32 s17, s39, 0
	s_add_u32 s18, s38, 0x4a00
	s_addc_u32 s19, s39, 0
	s_add_u32 s20, s38, 0x4b00
	s_addc_u32 s21, s39, 0
	s_add_u32 s22, s38, 0x4c00
	s_addc_u32 s23, s39, 0
	s_add_u32 s24, s38, 0x4d00
	s_addc_u32 s25, s39, 0
	s_add_u32 s26, s38, 0x4e00
	s_addc_u32 s27, s39, 0
	s_add_u32 s28, s38, 0x4f00
	s_addc_u32 s29, s39, 0
	s_add_u32 s30, s38, 0x5000
	s_addc_u32 s31, s39, 0
	s_add_u32 s34, s38, 0x5100
	s_addc_u32 s35, s39, 0
	v_readlane_b32 s37, v252, 3
	s_add_u32 s36, s38, 0x5200
	s_addc_u32 s37, s39, 0
	s_add_u32 s38, s38, 0x5300
	s_addc_u32 s39, s39, 0
	s_mov_b32 s46, 1
	v_mov_b32_e32 v17, 0
	s_branch .LBB0_1007
